# nt hint also on the phase-0 x (f32 -> e4m3) stream loads; otherwise as previous best (pipelined nt weight-conversion loads, sparse L0 bias table + VALU trims, L1 dense dword-store epilogue)
# speedup vs baseline: 1.0135x; 1.0135x over previous
; #define PIN(i) ((const float*)(__attribute__((address_space(1))) const float*)ka[i])
; __device__ __forceinline__ void phase_prologue(kcu64_t* ka, unsigned char* ws, LAS unsigned char* lds, int G, int bid, int tid, int jlo, int jhi, bool do_x) {
;     ...
;     if (do_x) { const f32x8* xs = (const f32x8*)PIN(I_X); const size_t n8 = (size_t)T_ * DM / 8;
;       if constexpr (F8_IN) { u32x2* xd = (u32x2*)(ws + WS_RC + 64 * MiB);
;           for (size_t i = (size_t)bid * NTHR + tid; i < n8; i += (size_t)G * NTHR) { const f32x8 v = xs[i]; xd[i] = (u32x2){pk4_fp8(v[0], v[1], v[2], v[3]), pk4_fp8(v[4], v[5], v[6], v[7])}; } }
.LBB0_24:
	global_load_dwordx4 v[6:9], v[4:5], off offset:16 nt
	global_load_dwordx4 v[10:13], v[4:5], off nt
	v_lshl_add_u64 v[2:3], v[2:3], 0, s[66:67]
	s_mov_b64 s[2:3], 0x7fffff
	v_cmp_lt_u64_e32 vcc, s[2:3], v[2:3]
	v_lshl_add_u64 v[4:5], v[4:5], 0, s[28:29]
	s_or_b64 s[0:1], vcc, s[0:1]
	s_waitcnt vmcnt(1)
	v_cvt_pk_fp8_f32 v6, v6, v7
	s_waitcnt vmcnt(0)
	v_cvt_pk_fp8_f32 v10, v10, v11
	v_cvt_pk_fp8_f32 v6, v8, v9 op_sel:[0,0,1]
	v_cvt_pk_fp8_f32 v10, v12, v13 op_sel:[0,0,1]
	v_mov_b32_e32 v11, v6
	global_store_dwordx2 v[0:1], v[10:11], off
	v_lshl_add_u64 v[0:1], v[0:1], 0, s[24:25]
	s_andn2_b64 exec, exec, s[0:1]
	s_cbranch_execnz .LBB0_24
